# dil H1: bias built in place + compare-based masks; FoX accumulator copies hoisted out of the tile loop; attention output stores global
# speedup vs baseline: 1.0239x; 1.0239x over previous
; __device__ __forceinline__ unsigned cvtpk(float lo, float hi) { f32x2_t v = {lo, hi}; bf16x2_t b = __builtin_convertvector(v, bf16x2_t); return __builtin_bit_cast(unsigned, b); }
; __device__ __forceinline__ s16x4 vtr(lds_cptr p) { return __builtin_bit_cast(s16x4, __builtin_amdgcn_ds_read_tr16_b64_v4i16((__attribute__((address_space(3))) v4i16_t*)p)); }
; template <class BIAS>
; __device__ __forceinline__ void attn_tiles(char* shm, const UnitIO& io, int t_begin, int t_end, const BIAS& B, int tid) {
;     ...
;         if (act) {
;             const lds_cptr vp = vp0 + sl_c;
;             s16x4 vlo[8], vhi[8];
; #pragma unroll
;             for (int i = 0; i < 8; ++i) { vlo[i] = vtr(vp + (i >> 2) * 4096 + (i & 3) * 1024); vhi[i] = vtr(vp + (i >> 2) * 4096 + (i & 3) * 1024 + 512); }
;             ATT_SBAR();
;             { float s1 = 0.f;
; #pragma unroll
;               for (int r = 0; r < 16; ++r) c1x[r] = __builtin_amdgcn_exp2f(c1x[r]);
;               { f32x2_t s2 = (f32x2_t){c1x[0], c1x[1]};
; #pragma unroll
;                 for (int i = 1; i < 8; ++i) s2 += (f32x2_t){c1x[2 * i], c1x[2 * i + 1]};
;                 s1 = s2[0] + s2[1]; }
;               l_reg += s1;
; #pragma unroll
;               for (int i = 0; i < 4; ++i) { pw[2][i] = cvtpk(c1x[2 * i], c1x[2 * i + 1]); pw[3][i] = cvtpk(c1x[8 + 2 * i], c1x[9 + 2 * i]); } }
;             ATT_SBAR();
;             asm volatile("" : "+v"(vlo[0]), "+v"(vhi[0]), "+v"(vlo[1]), "+v"(vhi[1]), "+v"(vlo[2]), "+v"(vhi[2]), "+v"(vlo[3]), "+v"(vhi[3]));
; #pragma unroll
;             for (int ks = 0; ks < 4; ++ks) { const bf16x8 vf = (bf16x8){vlo[ks][0], vlo[ks][1], vlo[ks][2], vlo[ks][3], vhi[ks][0], vhi[ks][1], vhi[ks][2], vhi[ks][3]};
;                 o[0] = __builtin_amdgcn_mfma_f32_32x32x16_bf16(__builtin_bit_cast(bf16x8, pw[ks]), vf, o[0], 0, 0, 0); }
;             ATT_SBAR();
;             asm volatile("" : "+v"(vlo[4]), "+v"(vhi[4]), "+v"(vlo[5]), "+v"(vhi[5]), "+v"(vlo[6]), "+v"(vhi[6]), "+v"(vlo[7]), "+v"(vhi[7]));
; #pragma unroll
;             for (int ks = 0; ks < 4; ++ks) { const bf16x8 vf = (bf16x8){vlo[4 + ks][0], vlo[4 + ks][1], vlo[4 + ks][2], vlo[4 + ks][3], vhi[4 + ks][0], vhi[4 + ks][1], vhi[4 + ks][2], vhi[4 + ks][3]};
;                 o[1] = __builtin_amdgcn_mfma_f32_32x32x16_bf16(__builtin_bit_cast(bf16x8, pw[ks]), vf, o[1], 0, 0, 0); }
;         }
.LBB0_355:
	v_add_u32_e32 v120, s20, v180
	ds_read_b64_tr_b16 v[74:75], v120 offset:32768
	ds_read_b64_tr_b16 v[76:77], v120 offset:33280
	ds_read_b64_tr_b16 v[78:79], v120 offset:33792
	ds_read_b64_tr_b16 v[80:81], v120 offset:34304
	ds_read_b64_tr_b16 v[98:99], v120 offset:34816
	ds_read_b64_tr_b16 v[100:101], v120 offset:35328
	ds_read_b64_tr_b16 v[102:103], v120 offset:35840
	ds_read_b64_tr_b16 v[104:105], v120 offset:36352
	ds_read_b64_tr_b16 v[106:107], v120 offset:36864
	ds_read_b64_tr_b16 v[108:109], v120 offset:37376
	ds_read_b64_tr_b16 v[110:111], v120 offset:37888
	ds_read_b64_tr_b16 v[112:113], v120 offset:38400
	ds_read_b64_tr_b16 v[114:115], v120 offset:38912
	ds_read_b64_tr_b16 v[116:117], v120 offset:39424
	ds_read_b64_tr_b16 v[118:119], v120 offset:39936
	ds_read_b64_tr_b16 v[120:121], v120 offset:40448
	v_exp_f32_e32 v50, v50
	v_exp_f32_e32 v51, v51
	v_exp_f32_e32 v52, v52
	v_exp_f32_e32 v53, v53
	v_exp_f32_e32 v54, v54
	v_exp_f32_e32 v55, v55
	v_exp_f32_e32 v56, v56
	v_exp_f32_e32 v57, v57
	v_exp_f32_e32 v58, v58
	v_exp_f32_e32 v59, v59
	v_exp_f32_e32 v60, v60
	v_exp_f32_e32 v61, v61
	v_add_f32_e32 v122, v52, v50
	v_add_f32_e32 v123, v53, v51
	v_exp_f32_e32 v62, v62
	v_exp_f32_e32 v63, v63
	v_add_f32_e32 v122, v54, v122
	v_add_f32_e32 v123, v55, v123
	v_exp_f32_e32 v64, v64
	v_exp_f32_e32 v65, v65
	v_add_f32_e32 v122, v56, v122
	v_add_f32_e32 v123, v57, v123
	v_cvt_pk_bf16_f32 v126, v58, v59
	v_add_f32_e32 v122, v58, v122
	v_add_f32_e32 v123, v59, v123
	v_cvt_pk_bf16_f32 v127, v60, v61
	v_add_f32_e32 v122, v60, v122
	v_add_f32_e32 v123, v61, v123
	v_cvt_pk_bf16_f32 v124, v54, v55
	v_add_f32_e32 v122, v62, v122
	v_add_f32_e32 v123, v63, v123
	v_cvt_pk_bf16_f32 v128, v62, v63
	v_add_f32_e32 v122, v64, v122
	v_add_f32_e32 v123, v65, v123
	v_cvt_pk_bf16_f32 v125, v56, v57
	v_add_f32_e32 v139, v122, v123
	v_cvt_pk_bf16_f32 v122, v50, v51
	v_cvt_pk_bf16_f32 v123, v52, v53
	v_cvt_pk_bf16_f32 v129, v64, v65
	s_waitcnt lgkmcnt(8)
	s_nop 0
	v_mfma_f32_32x32x16_bf16 v[12:27], v[66:69], v[74:77], v[12:27]
	v_mfma_f32_32x32x16_bf16 v[12:27], v[70:73], v[78:81], v[12:27]
	v_mfma_f32_32x32x16_bf16 v[12:27], v[122:125], v[98:101], v[12:27]
	v_mfma_f32_32x32x16_bf16 v[12:27], v[126:129], v[102:105], v[12:27]
	s_waitcnt lgkmcnt(0)
	v_add_f32_e32 v135, v135, v139
	v_mfma_f32_32x32x16_bf16 v[34:49], v[66:69], v[106:109], v[34:49]
	v_mfma_f32_32x32x16_bf16 v[34:49], v[70:73], v[110:113], v[34:49]
	v_mfma_f32_32x32x16_bf16 v[34:49], v[122:125], v[114:117], v[34:49]
	v_mfma_f32_32x32x16_bf16 v[34:49], v[126:129], v[118:121], v[34:49]
	s_mov_b64 s[34:35], -1
	s_and_b64 vcc, exec, s[46:47]
	s_cbranch_vccnz .LBB0_349

; #define ATT_WAIT_BAR(N) asm volatile("s_waitcnt vmcnt(" #N ") lgkmcnt(0)\n\ts_barrier" ::: "memory")
; #define ATT_DMA(t, slot) do { glds16(ksrc + (long)(t) * tstep, (unsigned)__builtin_amdgcn_readfirstlane(kdst + (slot))); glds16(vsrc + (long)(t) * tstep, (unsigned)__builtin_amdgcn_readfirstlane(vdst + (slot))); } while (0)
; template <class BIAS>
; __device__ __forceinline__ void attn_tiles(char* shm, const UnitIO& io, int t_begin, int t_end, const BIAS& B, int tid) {
;     ...
; #pragma unroll 1
;     for (int t = t_begin; t < t_end; ++t) {
;         const int rem = t_end - t;
;         const bool act = B.active(t);
;         const int sl_c = ((t - t_begin) & 3) * SLOTB;
;         if (rem > 3) ATT_DMA(t + 3, ((t + 3 - t_begin) & 3) * SLOTB);
;     ...
;         if (rem > 3) ATT_WAIT_BAR(4); else if (rem > 2) ATT_WAIT_BAR(2); else ATT_WAIT_BAR(0);
;     }
.LBB0_358:
	s_addk_i32 s39, 0x2000
	s_add_i32 s20, s44, 1
	s_add_i32 s21, s44, -2
	s_add_i32 s38, s38, -1
	s_cmp_ge_i32 s21, s26
	v_add_u32_e32 v137, 0x100, v137
	s_cbranch_scc0 .LBB0_340
	s_nop 11
	v_mov_b32_e32 v202, v12
	v_mov_b32_e32 v200, v13
	v_mov_b32_e32 v198, v14
	v_mov_b32_e32 v196, v15
	v_mov_b32_e32 v176, v16
	v_mov_b32_e32 v174, v17
	v_mov_b32_e32 v172, v18
	v_mov_b32_e32 v170, v19
	v_mov_b32_e32 v169, v20
	v_mov_b32_e32 v167, v21
	v_mov_b32_e32 v153, v22
	v_mov_b32_e32 v149, v23
	v_mov_b32_e32 v168, v24
	v_mov_b32_e32 v166, v25
	v_mov_b32_e32 v151, v26
	v_mov_b32_e32 v139, v27
	v_mov_b32_e32 v211, v34
	v_mov_b32_e32 v210, v35
	v_mov_b32_e32 v209, v36
	v_mov_b32_e32 v208, v37
	v_mov_b32_e32 v207, v38
	v_mov_b32_e32 v206, v39
	v_mov_b32_e32 v205, v40
	v_mov_b32_e32 v204, v41
	v_mov_b32_e32 v203, v42
	v_mov_b32_e32 v201, v43
	v_mov_b32_e32 v199, v44
	v_mov_b32_e32 v197, v45
	v_mov_b32_e32 v177, v46
	v_mov_b32_e32 v175, v47
	v_mov_b32_e32 v173, v48
	v_mov_b32_e32 v171, v49

; #pragma unroll
;         for (int i = 0; i < 8; ++i) { const int r = 2 * i; kc[i] = (f32x2_t){sd * (float)((r & 3) + 8 * (r >> 2)), sd * (float)(((r + 1) & 3) + 8 * ((r + 1) >> 2))}; } }
;     __device__ __forceinline__ void init(f32x16& c0, f32x16& c1, int t) const {
;         const int dt = t - (w >> 1);
;         const float base = basel + (float)dt * d64;
; #pragma unroll
;         for (int i = 0; i < 8; ++i) { const f32x2_t p = kc[i] + base, q = p + d32; c0[2 * i] = p[0]; c0[2 * i + 1] = p[1]; c1[2 * i] = q[0]; c1[2 * i + 1] = q[1]; }
;         if (dt == 0) {
; #pragma unroll
;             for (int r = 0; r < 16; ++r) { const int ko = (r & 3) + 8 * (r >> 2); if (ko < u) c0[r] = ATT_NEG; if (ko < u - 32) c1[r] = ATT_NEG; }
;         } else if (dt == 2) {
; #pragma unroll
;             for (int r = 0; r < 16; ++r) { const int ko = (r & 3) + 8 * (r >> 2); if (ko > u) c0[r] = ATT_NEG; if (ko > u - 32) c1[r] = ATT_NEG; }
;         }
;     }
.LBB0_367:
	s_cmp_ge_i32 s88, s73
	s_cselect_b64 s[56:57], -1, 0
	s_cmp_le_i32 s88, s33
	s_cselect_b64 s[70:71], -1, 0
	s_and_b64 s[70:71], s[56:57], s[70:71]
	s_add_i32 s56, s81, 0xffffa000
	v_cndmask_b32_e64 v58, 0, 1, s[70:71]
	s_and_b32 s82, s56, 0x6000
	v_cmp_ne_u32_e64 s[56:57], 1, v58
	s_andn2_b64 vcc, exec, s[70:71]
	s_cbranch_vccnz .LBB0_374
	v_add_u32_e32 v34, s82, v181
	ds_read_b128 v[130:133], v34
	ds_read_b128 v[126:129], v34 offset:512
	ds_read_b128 v[134:137], v34 offset:2048
	ds_read_b128 v[122:125], v34 offset:2560
	ds_read_b128 v[138:141], v34 offset:4096
	ds_read_b128 v[118:121], v34 offset:4608
	ds_read_b128 v[142:145], v34 offset:6144
	ds_read_b128 v[114:117], v34 offset:6656
	s_add_u32 s70, s72, s88
	v_cvt_f32_i32_e32 v34, s70
	v_mov_b32_e32 v157, v156
	v_fma_f32 v34, v149, v34, -v0
	v_add_f32_e32 v82, v154, v34
	v_add_f32_e32 v83, v155, v34
	v_add_f32_e32 v84, v158, v34
	v_add_f32_e32 v85, v159, v34
	v_add_f32_e32 v86, v160, v34
	v_add_f32_e32 v87, v161, v34
	v_add_f32_e32 v88, v162, v34
	v_add_f32_e32 v89, v163, v34
	v_add_f32_e32 v90, v164, v34
	v_add_f32_e32 v91, v165, v34
	v_add_f32_e32 v92, v166, v34
	v_add_f32_e32 v93, v167, v34
	v_add_f32_e32 v94, v168, v34
	v_add_f32_e32 v95, v169, v34
	v_add_f32_e32 v96, v170, v34
	v_add_f32_e32 v97, v171, v34
	v_add_f32_e32 v46, v156, v94
	v_add_f32_e32 v47, v157, v95
	v_add_f32_e32 v48, v156, v96
	v_add_f32_e32 v49, v157, v97
	v_add_f32_e32 v44, v156, v92
	v_add_f32_e32 v45, v157, v93
	v_add_f32_e32 v42, v156, v90
	v_add_f32_e32 v43, v157, v91
	v_add_f32_e32 v40, v156, v88
	v_add_f32_e32 v41, v157, v89
	v_add_f32_e32 v38, v156, v86
	v_add_f32_e32 v39, v157, v87
	v_add_f32_e32 v36, v156, v84
	v_add_f32_e32 v37, v157, v85
	v_add_f32_e32 v34, v176, v82
	v_add_f32_e32 v35, v177, v83
	s_cmp_eq_u32 s70, 1
	s_cbranch_scc1 .Ldil_h1_go
	s_cmp_eq_u32 s70, 0
	s_cbranch_scc0 .Ldil_m2
	v_cndmask_b32_e64 v82, v82, v226, s[6:7]
	v_cndmask_b32_e64 v83, v83, v226, s[10:11]
	v_cndmask_b32_e64 v84, v84, v226, s[14:15]
	v_cndmask_b32_e64 v85, v85, v226, s[18:19]
	v_cndmask_b32_e64 v86, v86, v226, s[22:23]
	v_cndmask_b32_e64 v87, v87, v226, s[26:27]
	v_cndmask_b32_e64 v88, v88, v226, s[92:93]
	v_cndmask_b32_e64 v89, v89, v226, s[96:97]
	v_cndmask_b32_e64 v90, v90, v226, s[4:5]
	v_cndmask_b32_e64 v91, v91, v226, s[60:61]
	v_cndmask_b32_e64 v92, v92, v226, s[30:31]
	v_cndmask_b32_e64 v93, v93, v226, s[58:59]
	v_cndmask_b32_e64 v94, v94, v226, s[40:41]
	v_cndmask_b32_e64 v95, v95, v226, s[44:45]
	v_cndmask_b32_e64 v96, v96, v226, s[48:49]
	v_cndmask_b32_e64 v34, v34, v226, s[8:9]
	v_cndmask_b32_e64 v35, v35, v226, s[12:13]
	v_cndmask_b32_e64 v36, v36, v226, s[16:17]
	v_cndmask_b32_e64 v37, v37, v226, s[20:21]
	v_cndmask_b32_e64 v38, v38, v226, s[24:25]
	v_cndmask_b32_e64 v39, v39, v226, s[90:91]
	v_cndmask_b32_e64 v40, v40, v226, s[94:95]
	v_cndmask_b32_e64 v41, v41, v226, s[34:35]
	v_cndmask_b32_e64 v42, v42, v226, s[0:1]
	v_cndmask_b32_e64 v43, v43, v226, s[28:29]
	v_cndmask_b32_e64 v44, v44, v226, s[36:37]
	v_cndmask_b32_e64 v45, v45, v226, s[38:39]
	v_cndmask_b32_e64 v46, v46, v226, s[42:43]
	v_cndmask_b32_e64 v47, v47, v226, s[46:47]
	v_cndmask_b32_e64 v48, v48, v226, s[50:51]
	v_cndmask_b32_e64 v97, v97, v226, s[52:53]
	v_cndmask_b32_e64 v49, v49, v226, s[54:55]
	s_branch .Ldil_h1_go
.Ldil_m2:
	s_and_b32 s2, s76, 1
	s_lshl_b32 s2, s2, 5
	v_lshrrev_b32_e32 v51, 3, v194
	v_and_b32_e32 v51, 4, v51
	v_add_u32_e32 v50, s2, v146
	v_sub_u32_e32 v50, v50, v51
	v_add_u32_e32 v51, 0xffffffe0, v50
	v_cmp_gt_i32_e64 s[2:3], 0, v50
	v_cmp_gt_i32_e64 s[70:71], 1, v50
	v_cmp_gt_i32_e64 s[84:85], 2, v50
	v_cndmask_b32_e64 v82, v82, v226, s[2:3]
	v_cndmask_b32_e64 v83, v83, v226, s[70:71]
	v_cndmask_b32_e64 v84, v84, v226, s[84:85]
	v_cmp_gt_i32_e64 s[2:3], 3, v50
	v_cmp_gt_i32_e64 s[70:71], 8, v50
	v_cmp_gt_i32_e64 s[84:85], 9, v50
	v_cndmask_b32_e64 v85, v85, v226, s[2:3]
	v_cndmask_b32_e64 v86, v86, v226, s[70:71]
	v_cndmask_b32_e64 v87, v87, v226, s[84:85]
	v_cmp_gt_i32_e64 s[2:3], 10, v50
	v_cmp_gt_i32_e64 s[70:71], 11, v50
	v_cmp_gt_i32_e64 s[84:85], 16, v50
	v_cndmask_b32_e64 v88, v88, v226, s[2:3]
	v_cndmask_b32_e64 v89, v89, v226, s[70:71]
	v_cndmask_b32_e64 v90, v90, v226, s[84:85]
	v_cmp_gt_i32_e64 s[2:3], 17, v50
	v_cmp_gt_i32_e64 s[70:71], 18, v50
	v_cmp_gt_i32_e64 s[84:85], 19, v50
	v_cndmask_b32_e64 v91, v91, v226, s[2:3]
	v_cndmask_b32_e64 v92, v92, v226, s[70:71]
	v_cndmask_b32_e64 v93, v93, v226, s[84:85]
	v_cmp_gt_i32_e64 s[2:3], 24, v50
	v_cmp_gt_i32_e64 s[70:71], 25, v50
	v_cmp_gt_i32_e64 s[84:85], 26, v50
	v_cndmask_b32_e64 v94, v94, v226, s[2:3]
	v_cndmask_b32_e64 v95, v95, v226, s[70:71]
	v_cndmask_b32_e64 v96, v96, v226, s[84:85]
	v_cmp_gt_i32_e64 s[2:3], 27, v50
	v_cmp_gt_i32_e64 s[70:71], 0, v51
	v_cmp_gt_i32_e64 s[84:85], 1, v51
	v_cndmask_b32_e64 v97, v97, v226, s[2:3]
	v_cndmask_b32_e64 v34, v34, v226, s[70:71]
	v_cndmask_b32_e64 v35, v35, v226, s[84:85]
	v_cmp_gt_i32_e64 s[2:3], 2, v51
	v_cmp_gt_i32_e64 s[70:71], 3, v51
	v_cmp_gt_i32_e64 s[84:85], 8, v51
	v_cndmask_b32_e64 v36, v36, v226, s[2:3]
	v_cndmask_b32_e64 v37, v37, v226, s[70:71]
	v_cndmask_b32_e64 v38, v38, v226, s[84:85]
	v_cmp_gt_i32_e64 s[2:3], 9, v51
	v_cmp_gt_i32_e64 s[70:71], 10, v51
	v_cmp_gt_i32_e64 s[84:85], 11, v51
	v_cndmask_b32_e64 v39, v39, v226, s[2:3]
	v_cndmask_b32_e64 v40, v40, v226, s[70:71]
	v_cndmask_b32_e64 v41, v41, v226, s[84:85]
	v_cmp_gt_i32_e64 s[2:3], 16, v51
	v_cmp_gt_i32_e64 s[70:71], 17, v51
	v_cmp_gt_i32_e64 s[84:85], 18, v51
	v_cndmask_b32_e64 v42, v42, v226, s[2:3]
	v_cndmask_b32_e64 v43, v43, v226, s[70:71]
	v_cndmask_b32_e64 v44, v44, v226, s[84:85]
	v_cmp_gt_i32_e64 s[2:3], 19, v51
	v_cmp_gt_i32_e64 s[70:71], 24, v51
	v_cmp_gt_i32_e64 s[84:85], 25, v51
	v_cndmask_b32_e64 v45, v45, v226, s[2:3]
	v_cndmask_b32_e64 v46, v46, v226, s[70:71]
	v_cndmask_b32_e64 v47, v47, v226, s[84:85]
	v_cmp_gt_i32_e64 s[2:3], 26, v51
	v_cmp_gt_i32_e64 s[70:71], 27, v51
	s_nop 0
	v_cndmask_b32_e64 v48, v48, v226, s[2:3]
	v_cndmask_b32_e64 v49, v49, v226, s[70:71]
	s_branch .Ldil_h1_go

; __device__ __forceinline__ unsigned cvtpk(float lo, float hi) { f32x2_t v = {lo, hi}; bf16x2_t b = __builtin_convertvector(v, bf16x2_t); return __builtin_bit_cast(unsigned, b); }
; #define ATT_SBAR() __builtin_amdgcn_sched_barrier(0)
; template <class BIAS>
; __device__ __forceinline__ void attn_tiles(char* shm, const UnitIO& io, int t_begin, int t_end, const BIAS& B, int tid) {
;     ...
;             f32x16 c0, c1; B.init(c0, c1, t);
;             ATT_SBAR();
;             asm volatile("" : "+v"(kf[0]), "+v"(kf[1]), "+v"(kf[2]), "+v"(kf[3]), "+v"(kf[4]), "+v"(kf[5]), "+v"(kf[6]), "+v"(kf[7]));
; #pragma unroll
;             for (int d0 = 0; d0 < 4; ++d0) { c0 = __builtin_amdgcn_mfma_f32_32x32x16_bf16(kf[2 * d0], qr[d0], c0, 0, 0, 0); c1 = __builtin_amdgcn_mfma_f32_32x32x16_bf16(kf[2 * d0 + 1], qr[d0], c1, 0, 0, 0); }
;             float s0 = 0.f;
; #pragma unroll
;             for (int r = 0; r < 16; ++r) c0[r] = __builtin_amdgcn_exp2f(c0[r]);
;             { f32x2_t s2 = (f32x2_t){c0[0], c0[1]};
; #pragma unroll
;               for (int i = 1; i < 8; ++i) s2 += (f32x2_t){c0[2 * i], c0[2 * i + 1]};
;               s0 = s2[0] + s2[1]; }
;             l_reg += s0;
; #pragma unroll
;             for (int i = 0; i < 4; ++i) { pw[0][i] = cvtpk(c0[2 * i], c0[2 * i + 1]); pw[1][i] = cvtpk(c0[8 + 2 * i], c0[9 + 2 * i]); }
;             c1x = c1;
.Ldil_h1_go:
	s_waitcnt lgkmcnt(0)
	s_nop 0
	v_mfma_f32_32x32x16_bf16 v[82:97], v[130:133], v[98:101], v[82:97]
	v_mfma_f32_32x32x16_bf16 v[82:97], v[134:137], v[102:105], v[82:97]
	v_mfma_f32_32x32x16_bf16 v[34:49], v[126:129], v[98:101], v[34:49]
	v_mfma_f32_32x32x16_bf16 v[82:97], v[138:141], v[106:109], v[82:97]
	v_mfma_f32_32x32x16_bf16 v[34:49], v[122:125], v[102:105], v[34:49]
	v_mfma_f32_32x32x16_bf16 v[82:97], v[142:145], v[110:113], v[82:97]
	v_mfma_f32_32x32x16_bf16 v[34:49], v[118:121], v[106:109], v[34:49]
	s_nop 10
	v_exp_f32_e32 v50, v82
	v_exp_f32_e32 v51, v83
	v_exp_f32_e32 v52, v84
	v_exp_f32_e32 v53, v85
	v_exp_f32_e32 v56, v86
	v_exp_f32_e32 v57, v87
	v_exp_f32_e32 v58, v88
	v_exp_f32_e32 v59, v89
	v_exp_f32_e32 v54, v90
	v_exp_f32_e32 v55, v91
	v_exp_f32_e32 v60, v92
	v_exp_f32_e32 v61, v93
	v_add_f32_e32 v66, v50, v52
	v_add_f32_e32 v67, v51, v53
	v_exp_f32_e32 v62, v94
	v_exp_f32_e32 v63, v95
	v_add_f32_e32 v66, v56, v66
	v_add_f32_e32 v67, v57, v67
	v_mfma_f32_32x32x16_bf16 v[34:49], v[114:117], v[110:113], v[34:49]
	v_exp_f32_e32 v64, v96
	v_exp_f32_e32 v65, v97
	v_add_f32_e32 v66, v58, v66
	v_add_f32_e32 v67, v59, v67
	v_cvt_pk_bf16_f32 v50, v50, v51
	v_add_f32_e32 v66, v54, v66
	v_add_f32_e32 v67, v55, v67
	v_cvt_pk_bf16_f32 v54, v54, v55
	v_add_f32_e32 v66, v60, v66
	v_add_f32_e32 v67, v61, v67
	v_cvt_pk_bf16_f32 v51, v52, v53
	v_add_f32_e32 v66, v62, v66
	v_add_f32_e32 v67, v63, v67
	v_cvt_pk_bf16_f32 v55, v60, v61
	v_add_f32_e32 v66, v64, v66
	v_add_f32_e32 v67, v65, v67
	v_cvt_pk_bf16_f32 v52, v56, v57
	v_add_f32_e32 v66, v66, v67
	v_cvt_pk_bf16_f32 v56, v62, v63
	v_cvt_pk_bf16_f32 v53, v58, v59
	v_cvt_pk_bf16_f32 v57, v64, v65
	v_add_f32_e32 v151, v151, v66
	s_and_b64 vcc, exec, s[56:57]
	s_cbranch_vccz .LBB0_375

; #define ATT_WAIT_BAR(N) asm volatile("s_waitcnt vmcnt(" #N ") lgkmcnt(0)\n\ts_barrier" ::: "memory")
; __device__ __forceinline__ int crow(int r, int hi) { return (r & 3) + 8 * (r >> 2) + 4 * hi; }
; template <class BIAS>
; __device__ __forceinline__ void attn_tiles(char* shm, const UnitIO& io, int t_begin, int t_end, const BIAS& B, int tid) {
;     ...
;         if (rem > 3) ATT_WAIT_BAR(4); else if (rem > 2) ATT_WAIT_BAR(2); else ATT_WAIT_BAR(0);
;     }
;     ...
;     { auto rr = __builtin_amdgcn_permlane32_swap(__float_as_uint(l_reg), __float_as_uint(l_reg), false, false); l_reg = __uint_as_float(rr[0]) + __uint_as_float(rr[1]); }
;     if (hi == 0) wsf[32 + r32] = l_reg;
;     asm volatile("s_waitcnt lgkmcnt(0)" ::: "memory");
;     float rli[16];
; #pragma unroll
;     for (int r = 0; r < 16; ++r) rli[r] = io.norm ? __builtin_amdgcn_rcpf(wsf[32 + crow(r, hi)]) : 1.0f;
;     if (!io.norm && hi == 0) io.L[(long)r32 * io.lstride] = l_reg;
.LBB0_387:
	s_waitcnt vmcnt(4) lgkmcnt(0)
	s_barrier
	s_branch .LBB0_364
.LBB0_389:
	v_mov_b32_e32 v0, v151
	s_nop 1
	v_permlane32_swap_b32_e32 v151, v0
	v_readlane_b32 s2, v255, 3
	v_add_f32_e32 v34, v151, v0
	v_readlane_b32 s3, v255, 4
	s_and_saveexec_b64 s[56:57], s[2:3]
	s_and_b32 s68, s77, 0x3fffffc0
	v_lshl_or_b32 v0, s68, 2, v197
	v_add_u32_e32 v0, 0x10080, v0
	ds_write_b32 v0, v34
	s_or_b64 exec, exec, s[56:57]
	s_waitcnt lgkmcnt(0)
	v_readlane_b32 s2, v255, 3
	v_readlane_b32 s3, v255, 4
	s_and_saveexec_b64 s[56:57], s[2:3]
	s_cbranch_execz .LBB0_362
	v_readlane_b32 s2, v254, 9
	v_readlane_b32 s3, v254, 10
	s_lshl_b64 s[68:69], s[66:67], 5
	s_lshl_b64 s[70:71], s[2:3], 20
	v_readlane_b32 s2, v255, 21
	s_add_u32 s70, s2, s70
	v_readlane_b32 s2, v255, 22
	s_addc_u32 s71, s2, s71
	s_add_u32 s68, s70, s68
	s_addc_u32 s69, s71, s69
	s_lshl_b32 s70, s75, 2
	s_add_u32 s68, s68, s70
	s_addc_u32 s69, s69, 0
	s_and_b64 s[70:71], s[64:65], exec
	s_cselect_b32 s75, 5, 7
	s_and_b64 s[70:71], s[62:63], exec
	s_cselect_b32 s70, 3, s75
	v_lshlrev_b32_e32 v0, s70, v146
	v_lshlrev_b32_e32 v0, 2, v0
	v_lshl_add_u64 v[36:37], s[68:69], 0, v[0:1]
	flat_store_dword v[36:37], v34
	s_branch .LBB0_362
